# attention micro-edits combined on v030: tile-top ds_reads first, packed-to-scalar fp32, back-edge rotation, scalar form of the no-next-tile flag (s_not_b64 instead of v_cndmask+v_cmp)
# speedup vs baseline: 1.0125x; 1.0015x over previous
; #define LAS __attribute__((address_space(3)))
; __device__ __forceinline__ void qkt(f32x16& p0, f32x16& p1, const LAS char* Ks, const bf16x8* qr, int r32, int hi) {
;   p0 = f32x16{}; p1 = f32x16{};
; #pragma unroll
;   for (int d0 = 0; d0 < 8; ++d0) { int cb = (d0 * 16 + hi * 8) * 2;
;     bf16x8 b0 = *(const LAS bf16x8*)(Ks + KSWZ(r32, cb));
;     bf16x8 b1 = *(const LAS bf16x8*)(Ks + KSWZ(32 + r32, cb));
;     p0 = __builtin_amdgcn_mfma_f32_32x32x16_bf16(b0, qr[d0], p0, 0, 0, 0);
;     p1 = __builtin_amdgcn_mfma_f32_32x32x16_bf16(b1, qr[d0], p1, 0, 0, 0); }
; }
.LBB0_936:
	s_waitcnt lgkmcnt(3)
	v_mfma_f32_32x32x16_bf16 v[148:163], v[132:135], v[164:167], 0
	s_mov_b32 s8, 0x42b504f3
	s_waitcnt lgkmcnt(2)
	v_mfma_f32_32x32x16_bf16 v[132:147], v[136:139], v[164:167], 0
	s_waitcnt lgkmcnt(1)
	v_mfma_f32_32x32x16_bf16 v[148:163], v[250:253], v[168:171], v[148:163]
	ds_read_b128 v[250:253], v246 offset:8192
	s_waitcnt lgkmcnt(1)
	v_mfma_f32_32x32x16_bf16 v[132:147], v[222:225], v[168:171], v[132:147]
	ds_read_b128 v[222:225], v246
	v_add_u32_e32 v246, v2, v235
	s_waitcnt lgkmcnt(1)
	v_mfma_f32_32x32x16_bf16 v[132:147], v[250:253], v[172:175], v[132:147]
	ds_read_b128 v[250:253], v246 offset:8192
	s_waitcnt lgkmcnt(1)
	v_mfma_f32_32x32x16_bf16 v[148:163], v[222:225], v[172:175], v[148:163]
	ds_read_b128 v[222:225], v246
	v_add_u32_e32 v246, v2, v236
	s_waitcnt lgkmcnt(1)
	v_mfma_f32_32x32x16_bf16 v[132:147], v[250:253], v[176:179], v[132:147]
	ds_read_b128 v[250:253], v246 offset:8192
	s_waitcnt lgkmcnt(1)
	v_mfma_f32_32x32x16_bf16 v[148:163], v[222:225], v[176:179], v[148:163]
	ds_read_b128 v[222:225], v246
	v_add_u32_e32 v246, v2, v237
	s_waitcnt lgkmcnt(1)
	v_mfma_f32_32x32x16_bf16 v[132:147], v[250:253], v[180:183], v[132:147]
	ds_read_b128 v[250:253], v246 offset:8192
	s_waitcnt lgkmcnt(1)
	v_mfma_f32_32x32x16_bf16 v[148:163], v[222:225], v[180:183], v[148:163]
	ds_read_b128 v[222:225], v246
	v_add_u32_e32 v246, v2, v238
	v_add_u32_e32 v2, v2, v242
	s_waitcnt lgkmcnt(1)
	v_mfma_f32_32x32x16_bf16 v[132:147], v[250:253], v[184:187], v[132:147]
	ds_read_b128 v[250:253], v246 offset:8192
	s_waitcnt lgkmcnt(1)
	v_mfma_f32_32x32x16_bf16 v[148:163], v[222:225], v[184:187], v[148:163]
	ds_read_b128 v[222:225], v246
	s_waitcnt lgkmcnt(1)
	v_mfma_f32_32x32x16_bf16 v[132:147], v[250:253], v[188:191], v[132:147]
	ds_read_b128 v[250:253], v2 offset:8192
	s_waitcnt lgkmcnt(1)
	v_mfma_f32_32x32x16_bf16 v[148:163], v[222:225], v[188:191], v[148:163]
	ds_read_b128 v[222:225], v2
	s_waitcnt lgkmcnt(0)
; #define SBAR() __builtin_amdgcn_sched_barrier(0)
; #define SLOAD_A(k0) do { const bf16_t* vp_ = Vh + (long)(k0) * LDK + toff; const bf16_t* kp_ = Kh + (long)(k0) * LDK + toff; \
;     sa0 = *(const bf16x8*)kp_; sa1 = *(const bf16x8*)(kp_ + 32L * LDK); sa2 = *(const bf16x8*)vp_; sa3 = *(const bf16x8*)(vp_ + 128); } while (0)
; __device__ __forceinline__ void partialSM(f32x16& p0, f32x16& p1, float& m_reg, float& mn, float& alpha) {
;   constexpr float C = SCALE * 1.4426950408889634f;
;   float pmax = p0[0]; for (int r = 1; r < 16; ++r) pmax = fmaxf(pmax, p0[r]); for (int r = 0; r < 16; ++r) pmax = fmaxf(pmax, p1[r]);
;   { auto rr = __builtin_amdgcn_permlane32_swap(__float_as_uint(pmax), __float_as_uint(pmax), false, false);
;     pmax = fmaxf(__uint_as_float(rr[0]), __uint_as_float(rr[1])); }
;   if (__builtin_expect(__all(pmax - m_reg <= THR / SCALE), 1)) { mn = m_reg; alpha = 1.f; }
;   else { mn = fmaxf(m_reg, pmax); alpha = __builtin_amdgcn_exp2f((m_reg - mn) * C); m_reg = mn; }
;   float mnC = -mn * C;
;   for (int r = 0; r < 16; ++r) p0[r] = fmaf(p0[r], C, mnC); for (int r = 0; r < 16; ++r) p1[r] = fmaf(p1[r], C, mnC);
;   for (int r = 0; r < 16; ++r) p0[r] = __builtin_amdgcn_exp2f(p0[r]);
; }
; __device__ __forceinline__ void finishSM(f32x16& p0, f32x16& p1, float alpha, float& l_reg, bf16x8& pa0, bf16x8& pa1, bf16x8& pa2, bf16x8& pa3) {
;   for (int r = 0; r < 16; ++r) p1[r] = __builtin_amdgcn_exp2f(p1[r]);
;   float ps = 0; for (int r = 0; r < 16; ++r) ps += p0[r]; for (int r = 0; r < 16; ++r) ps += p1[r];
;   { auto rr = __builtin_amdgcn_permlane32_swap(__float_as_uint(ps), __float_as_uint(ps), false, false);
;     ps = __uint_as_float(rr[0]) + __uint_as_float(rr[1]); }
;   l_reg = l_reg * alpha + ps;
;     ...
;   PK4(p0, 0, pa0); PK4(p0, 8, pa1); PK4(p1, 0, pa2); PK4(p1, 8, pa3);
;     ...
; }
; template <int LDQ, int LDK, int LDO>
; __device__ __forceinline__ void attn_body256(const bf16_t* __restrict__ Qb, const bf16_t* __restrict__ Kh, const bf16_t* __restrict__ Vh, float* __restrict__ Ob, int seq, LAS char* lds) {
;     ...
;     if (j + 1 < NT) SLOAD_A((j + 1) * KVBLK);
;     SBAR(); qkt(p0, p1, K_lds + (j & 1) * SHM_K2, qr, r32, hi);
;     partialSM(p0, p1, m_reg, mn, al);
;     finishSM(p0, p1, al, l_reg, pa0, pa1, pa2, pa3); SBAR();
;     if (j + 1 < NT) { asm volatile("s_waitcnt vmcnt(0)" ::: "memory"); SWRITE_A((j + 1) & 1); SLOAD_B((j + 1) * KVBLK); }
	v_mfma_f32_32x32x16_bf16 v[148:163], v[222:225], v[192:195], v[148:163]
	v_mfma_f32_32x32x16_bf16 v[132:147], v[250:253], v[192:195], v[132:147]
	s_nop 9
	v_max_f32_e32 v2, v149, v149
	v_max_f32_e32 v222, v148, v148
	v_max_f32_e32 v2, v222, v2
	v_max3_f32 v2, v2, v150, v151
	v_max3_f32 v2, v2, v152, v153
	v_max3_f32 v2, v2, v154, v155
	v_max3_f32 v2, v2, v156, v157
	v_max3_f32 v2, v2, v158, v159
	v_max3_f32 v2, v2, v160, v161
	v_max3_f32 v2, v2, v162, v163
	v_max3_f32 v2, v2, v132, v133
	v_max3_f32 v2, v2, v134, v135
	v_max3_f32 v2, v2, v136, v137
	v_max3_f32 v2, v2, v138, v139
	v_max3_f32 v2, v2, v140, v141
	v_max3_f32 v2, v2, v142, v143
	v_max3_f32 v2, v2, v144, v145
	v_max3_f32 v2, v2, v146, v147
	v_mov_b32_e32 v222, v2
	s_nop 1
	v_permlane32_swap_b32_e32 v2, v222
	v_max_f32_e32 v222, v222, v222
	v_max_f32_e32 v2, v2, v2
	v_max_f32_e32 v2, v2, v222
	v_sub_f32_e32 v222, v2, v248
	v_cmp_ge_f32_e32 vcc, s8, v222
	s_cmp_eq_u64 vcc, exec
	v_max_f32_e32 v222, v248, v248
	s_cselect_b64 s[10:11], -1, 0
	v_max_f32_e32 v249, v222, v2
	v_cndmask_b32_e64 v2, v249, v248, s[10:11]
	v_mul_f32_e32 v222, 0xbe0293ee, v2
	v_fmamk_f32 v148, v148, 0x3e0293ee, v222
	v_fmamk_f32 v149, v149, 0x3e0293ee, v222
	v_fmamk_f32 v150, v150, 0x3e0293ee, v222
	v_fmamk_f32 v151, v151, 0x3e0293ee, v222
	v_fmamk_f32 v152, v152, 0x3e0293ee, v222
	v_fmamk_f32 v153, v153, 0x3e0293ee, v222
	v_fmamk_f32 v154, v154, 0x3e0293ee, v222
	v_fmamk_f32 v155, v155, 0x3e0293ee, v222
	v_fmamk_f32 v156, v156, 0x3e0293ee, v222
	v_fmamk_f32 v157, v157, 0x3e0293ee, v222
	v_fmamk_f32 v158, v158, 0x3e0293ee, v222
	v_fmamk_f32 v159, v159, 0x3e0293ee, v222
	v_fmamk_f32 v160, v160, 0x3e0293ee, v222
	v_fmamk_f32 v161, v161, 0x3e0293ee, v222
	v_fmamk_f32 v162, v162, 0x3e0293ee, v222
	v_fmamk_f32 v163, v163, 0x3e0293ee, v222
	v_fmamk_f32 v132, v132, 0x3e0293ee, v222
	v_fmamk_f32 v133, v133, 0x3e0293ee, v222
	v_fmamk_f32 v134, v134, 0x3e0293ee, v222
	v_fmamk_f32 v135, v135, 0x3e0293ee, v222
	v_fmamk_f32 v136, v136, 0x3e0293ee, v222
	v_fmamk_f32 v137, v137, 0x3e0293ee, v222
	v_fmamk_f32 v138, v138, 0x3e0293ee, v222
	v_fmamk_f32 v139, v139, 0x3e0293ee, v222
	v_fmamk_f32 v140, v140, 0x3e0293ee, v222
	v_fmamk_f32 v141, v141, 0x3e0293ee, v222
	v_fmamk_f32 v142, v142, 0x3e0293ee, v222
	v_fmamk_f32 v143, v143, 0x3e0293ee, v222
	v_fmamk_f32 v144, v144, 0x3e0293ee, v222
	v_fmamk_f32 v145, v145, 0x3e0293ee, v222
	v_fmamk_f32 v146, v146, 0x3e0293ee, v222
	v_fmac_f32_e32 v222, 0x3e0293ee, v147
	v_exp_f32_e32 v147, v148
	v_exp_f32_e32 v148, v149
	v_exp_f32_e32 v149, v150
	v_exp_f32_e32 v150, v151
	v_exp_f32_e32 v151, v152
	v_exp_f32_e32 v152, v153
	v_exp_f32_e32 v153, v154
	v_exp_f32_e32 v154, v155
	v_exp_f32_e32 v155, v156
	v_exp_f32_e32 v156, v157
	v_exp_f32_e32 v157, v158
	v_exp_f32_e32 v158, v159
	v_exp_f32_e32 v159, v160
	v_exp_f32_e32 v160, v161
	v_exp_f32_e32 v161, v162
	v_exp_f32_e32 v162, v163
	v_exp_f32_e32 v163, v132
	v_add_f32_e32 v132, 0, v147
	v_add_f32_e32 v132, v148, v132
	v_add_f32_e32 v132, v149, v132
	v_add_f32_e32 v132, v150, v132
	v_add_f32_e32 v132, v151, v132
	v_add_f32_e32 v132, v152, v132
	v_add_f32_e32 v132, v153, v132
	v_add_f32_e32 v132, v154, v132
	v_add_f32_e32 v132, v155, v132
	v_add_f32_e32 v132, v156, v132
	v_add_f32_e32 v132, v157, v132
	v_add_f32_e32 v132, v158, v132
	v_add_f32_e32 v132, v159, v132
	v_exp_f32_e32 v223, v133
	v_add_f32_e32 v132, v160, v132
	v_exp_f32_e32 v224, v134
	v_add_f32_e32 v132, v161, v132
	v_exp_f32_e32 v225, v135
	v_add_f32_e32 v132, v162, v132
	v_exp_f32_e32 v250, v136
	v_add_f32_e32 v132, v163, v132
	v_exp_f32_e32 v251, v137
	v_add_f32_e32 v132, v223, v132
	v_exp_f32_e32 v252, v138
	v_add_f32_e32 v132, v224, v132
	v_exp_f32_e32 v253, v139
	v_add_f32_e32 v132, v225, v132
	v_exp_f32_e32 v254, v140
	v_add_f32_e32 v132, v250, v132
	v_exp_f32_e32 v0, v141
	v_add_f32_e32 v132, v251, v132
	v_exp_f32_e32 v1, v142
	v_add_f32_e32 v132, v252, v132
	v_exp_f32_e32 v227, v143
	v_add_f32_e32 v132, v253, v132
	v_exp_f32_e32 v228, v144
	v_add_f32_e32 v132, v254, v132
	v_exp_f32_e32 v229, v145
	v_add_f32_e32 v132, v0, v132
	v_exp_f32_e32 v230, v146
	v_add_f32_e32 v132, v1, v132
	v_exp_f32_e32 v222, v222
	v_add_f32_e32 v132, v227, v132
	v_add_f32_e32 v132, v228, v132
	v_add_f32_e32 v132, v229, v132
	v_add_f32_e32 v132, v230, v132
	v_add_f32_e32 v246, v222, v132
	v_mov_b32_e32 v247, v246
	v_cvt_pk_bf16_f32 v132, v147, v148
	v_cvt_pk_bf16_f32 v133, v149, v150
	v_cvt_pk_bf16_f32 v134, v151, v152
	v_cvt_pk_bf16_f32 v135, v153, v154
	v_cvt_pk_bf16_f32 v136, v155, v156
	v_cvt_pk_bf16_f32 v137, v157, v158
	v_cvt_pk_bf16_f32 v138, v159, v160
	v_cvt_pk_bf16_f32 v139, v161, v162
	v_cvt_pk_bf16_f32 v140, v163, v223
	v_cvt_pk_bf16_f32 v141, v224, v225
	v_cvt_pk_bf16_f32 v142, v250, v251
	v_cvt_pk_bf16_f32 v143, v252, v253
	v_cvt_pk_bf16_f32 v144, v254, v0
	v_cvt_pk_bf16_f32 v145, v1, v227
	v_cvt_pk_bf16_f32 v146, v228, v229
	v_cvt_pk_bf16_f32 v147, v230, v222
	s_nop 1
	v_permlane32_swap_b32_e32 v246, v247
	v_permlane32_swap_b32_e32 v132, v134
	v_permlane32_swap_b32_e32 v133, v135
	v_permlane32_swap_b32_e32 v136, v138
	v_permlane32_swap_b32_e32 v137, v139
	v_permlane32_swap_b32_e32 v140, v142
	v_permlane32_swap_b32_e32 v141, v143
	v_permlane32_swap_b32_e32 v144, v146
	v_permlane32_swap_b32_e32 v145, v147
	s_not_b64 s[8:9], s[84:85]
	s_andn2_b64 vcc, exec, s[84:85]
	s_cbranch_vccnz .LBB0_938
	s_and_b32 s84, s87, 1
	v_lshl_add_u32 v1, s84, 14, v240
	v_add_co_u32_e32 v148, vcc, 0x125000, v220
	s_waitcnt vmcnt(0)
	v_lshl_add_u32 v0, s84, 15, v241
	s_waitcnt vmcnt(1)
	ds_write_b128 v1, v[204:207]
	s_waitcnt vmcnt(0)
	ds_write_b128 v1, v[208:211] offset:8192
	s_waitcnt vmcnt(1)
	ds_write_b128 v0, v[196:199]
	s_waitcnt vmcnt(0)
	ds_write_b128 v0, v[200:203] offset:2048
	v_addc_co_u32_e32 v149, vcc, 0, v221, vcc
	global_load_dwordx4 v[204:207], v[148:149], off
	global_load_dwordx4 v[208:211], v[148:149], off offset:256
